# NA bias/QK/PV LDS-latency restructure, NA band shift in LDS with consecutive row pairs per CU, tconv8 sliding-window main loop, MoE epilogue vmcnt(0) drains removed, Hyena filter final loop prefetch d
# speedup vs baseline: 1.0145x; 1.0145x over previous
.LBB0_79:
	s_or_b64 exec, exec, s[8:9]
	s_waitcnt vmcnt(0)
	s_add_i32 s80, s80, s70
	s_cmpk_gt_i32 s80, 0xff
	s_cbranch_scc1 .LBB0_131

.LBB0_128:
	v_ashrrev_i32_e32 v27, 31, v26
	v_lshl_add_u64 v[0:1], v[26:27], 2, s[16:17]
	global_load_dword v0, v[0:1], off
	s_mov_b64 s[24:25], 0
	s_mov_b32 s26, s66
	v_lshl_add_u64 v[152:153], v[24:25], 0, s[24:25]
	global_load_dword v160, v[152:153], off
	v_add_co_u32_e32 v154, vcc, s64, v152
	s_nop 1
	v_addc_co_u32_e32 v155, vcc, 0, v153, vcc
	global_load_dword v162, v[154:155], off
	v_add_co_u32_e32 v156, vcc, s67, v152
	s_nop 1
	v_addc_co_u32_e32 v157, vcc, 0, v153, vcc
	global_load_dword v164, v[156:157], off
	v_add_co_u32_e32 v158, vcc, s68, v152
	s_nop 1
	v_addc_co_u32_e32 v159, vcc, 0, v153, vcc
	global_load_dword v166, v[158:159], off
	s_mov_b32 s98, 0xc000
	s_mov_b32 s99, 0
	v_lshl_add_u64 v[152:153], v[24:25], 0, s[98:99]
	global_load_dword v168, v[152:153], off
	v_add_co_u32_e32 v154, vcc, s64, v152
	s_nop 1
	v_addc_co_u32_e32 v155, vcc, 0, v153, vcc
	global_load_dword v170, v[154:155], off
	v_add_co_u32_e32 v156, vcc, s67, v152
	s_nop 1
	v_addc_co_u32_e32 v157, vcc, 0, v153, vcc
	global_load_dword v172, v[156:157], off
	v_add_co_u32_e32 v158, vcc, s68, v152
	s_nop 1
	v_addc_co_u32_e32 v159, vcc, 0, v153, vcc
	global_load_dword v174, v[158:159], off
	s_waitcnt vmcnt(8)
	v_mov_b32_e32 v1, v0
	v_mov_b32_e32 v2, v0
	v_mov_b32_e32 v3, v0
	v_mov_b32_e32 v38, v0
	v_mov_b32_e32 v39, v0
	v_mov_b32_e32 v36, v0
	v_mov_b32_e32 v37, v0
	v_mov_b32_e32 v34, v0
	v_mov_b32_e32 v35, v0
	v_mov_b32_e32 v32, v0
	v_mov_b32_e32 v33, v0
	v_mov_b32_e32 v30, v0
	v_mov_b32_e32 v31, v0
	v_mov_b32_e32 v28, v0
	v_mov_b32_e32 v29, v0
.LBB0_129:
	s_waitcnt vmcnt(4)
	v_mov_b32_e32 v130, v160
	v_mov_b32_e32 v132, v162
	v_mov_b32_e32 v134, v164
	v_mov_b32_e32 v224, v166
	s_add_u32 s98, s24, 0x18000
	s_sub_u32 s99, s98, 0xc0000
	s_cmp_ge_u32 s98, 0xc0000
	s_cselect_b32 s98, s99, s98
	s_mov_b32 s99, 0
	v_lshl_add_u64 v[152:153], v[24:25], 0, s[98:99]
	global_load_dword v160, v[152:153], off
	v_add_co_u32_e32 v154, vcc, s64, v152
	s_nop 1
	v_addc_co_u32_e32 v155, vcc, 0, v153, vcc
	global_load_dword v162, v[154:155], off
	v_add_co_u32_e32 v156, vcc, s67, v152
	s_nop 1
	v_addc_co_u32_e32 v157, vcc, 0, v153, vcc
	global_load_dword v164, v[156:157], off
	v_add_co_u32_e32 v158, vcc, s68, v152
	s_nop 1
	v_addc_co_u32_e32 v159, vcc, 0, v153, vcc
	global_load_dword v166, v[158:159], off
	v_mov_b32_e32 v65, s26
	ds_read_b128 v[66:69], v65
	ds_read_b128 v[70:73], v65 offset:256
	ds_read_b128 v[74:77], v65 offset:512
	ds_read_b128 v[78:81], v65 offset:768
	ds_read_b128 v[82:85], v65 offset:1024
	ds_read_b128 v[86:89], v65 offset:1280
	ds_read_b128 v[90:93], v65 offset:1536
	ds_read_b128 v[94:97], v65 offset:1792
	ds_read_b128 v[98:101], v65 offset:2048
	ds_read_b128 v[102:105], v65 offset:2304
	ds_read_b128 v[106:109], v65 offset:2560
	ds_read_b128 v[110:113], v65 offset:2816
	ds_read_b128 v[114:117], v65 offset:3072
	ds_read_b128 v[118:121], v65 offset:3328
	ds_read_b128 v[122:125], v65 offset:3584
	ds_read_b128 v[126:129], v65 offset:3840
	s_waitcnt lgkmcnt(14)
	v_mov_b32_e32 v136, v66
	v_mov_b32_e32 v137, v70
	s_waitcnt lgkmcnt(13)
	v_mov_b32_e32 v138, v74
	s_waitcnt lgkmcnt(12)
	v_mov_b32_e32 v139, v78
	s_waitcnt lgkmcnt(11)
	v_mov_b32_e32 v140, v82
	s_waitcnt lgkmcnt(10)
	v_mov_b32_e32 v141, v86
	s_waitcnt lgkmcnt(9)
	v_mov_b32_e32 v142, v90
	s_waitcnt lgkmcnt(8)
	v_mov_b32_e32 v143, v94
	s_waitcnt lgkmcnt(7)
	v_mov_b32_e32 v144, v98
	s_waitcnt lgkmcnt(6)
	v_mov_b32_e32 v145, v102
	s_waitcnt lgkmcnt(5)
	v_mov_b32_e32 v146, v106
	s_waitcnt lgkmcnt(4)
	v_mov_b32_e32 v147, v110
	s_waitcnt lgkmcnt(3)
	v_mov_b32_e32 v148, v114
	s_waitcnt lgkmcnt(2)
	v_mov_b32_e32 v149, v118
	s_waitcnt lgkmcnt(1)
	v_mov_b32_e32 v150, v122
	s_waitcnt lgkmcnt(0)
	v_mov_b32_e32 v151, v126
	s_add_i32 s26, s26, 16
	v_mov_b32_e32 v70, v67
	v_mov_b32_e32 v78, v75
	v_mov_b32_e32 v86, v83
	v_mov_b32_e32 v94, v91
	v_mov_b32_e32 v102, v99
	v_mov_b32_e32 v110, v107
	v_mov_b32_e32 v118, v115
	v_mov_b32_e32 v126, v123
	s_add_u32 s24, s24, 0xc000
	v_mov_b32_e32 v66, v68
	v_mov_b32_e32 v67, v72
	v_mov_b32_e32 v74, v76
	v_mov_b32_e32 v75, v80
	v_mov_b32_e32 v82, v84
	v_mov_b32_e32 v83, v88
	v_mov_b32_e32 v90, v92
	v_mov_b32_e32 v91, v96
	v_mov_b32_e32 v98, v100
	v_mov_b32_e32 v99, v104
	v_mov_b32_e32 v106, v108
	v_mov_b32_e32 v107, v112
	v_mov_b32_e32 v114, v116
	v_mov_b32_e32 v115, v120
	v_mov_b32_e32 v122, v124
	v_mov_b32_e32 v123, v128
	s_addc_u32 s25, s25, 0
	v_mov_b32_e32 v72, v69
	v_mov_b32_e32 v80, v77
	v_mov_b32_e32 v88, v85
	v_mov_b32_e32 v96, v93
	v_mov_b32_e32 v104, v101
	v_mov_b32_e32 v112, v109
	v_mov_b32_e32 v120, v117
	v_mov_b32_e32 v128, v125
	v_pk_fma_f32 v[0:1], v[130:131], v[136:137], v[0:1] op_sel_hi:[0,1,1]
	v_pk_fma_f32 v[2:3], v[130:131], v[138:139], v[2:3] op_sel_hi:[0,1,1]
	v_pk_fma_f32 v[38:39], v[130:131], v[140:141], v[38:39] op_sel_hi:[0,1,1]
	v_pk_fma_f32 v[36:37], v[130:131], v[142:143], v[36:37] op_sel_hi:[0,1,1]
	v_pk_fma_f32 v[34:35], v[130:131], v[144:145], v[34:35] op_sel_hi:[0,1,1]
	v_pk_fma_f32 v[32:33], v[130:131], v[146:147], v[32:33] op_sel_hi:[0,1,1]
	v_pk_fma_f32 v[30:31], v[130:131], v[148:149], v[30:31] op_sel_hi:[0,1,1]
	v_pk_fma_f32 v[28:29], v[130:131], v[150:151], v[28:29] op_sel_hi:[0,1,1]
	v_pk_fma_f32 v[0:1], v[132:133], v[70:71], v[0:1] op_sel_hi:[0,1,1]
	v_pk_fma_f32 v[2:3], v[132:133], v[78:79], v[2:3] op_sel_hi:[0,1,1]
	v_pk_fma_f32 v[38:39], v[132:133], v[86:87], v[38:39] op_sel_hi:[0,1,1]
	v_pk_fma_f32 v[36:37], v[132:133], v[94:95], v[36:37] op_sel_hi:[0,1,1]
	v_pk_fma_f32 v[34:35], v[132:133], v[102:103], v[34:35] op_sel_hi:[0,1,1]
	v_pk_fma_f32 v[32:33], v[132:133], v[110:111], v[32:33] op_sel_hi:[0,1,1]
	v_pk_fma_f32 v[30:31], v[132:133], v[118:119], v[30:31] op_sel_hi:[0,1,1]
	v_pk_fma_f32 v[28:29], v[132:133], v[126:127], v[28:29] op_sel_hi:[0,1,1]
	v_pk_fma_f32 v[0:1], v[134:135], v[66:67], v[0:1] op_sel_hi:[0,1,1]
	v_pk_fma_f32 v[2:3], v[134:135], v[74:75], v[2:3] op_sel_hi:[0,1,1]
	v_pk_fma_f32 v[38:39], v[134:135], v[82:83], v[38:39] op_sel_hi:[0,1,1]
	v_pk_fma_f32 v[36:37], v[134:135], v[90:91], v[36:37] op_sel_hi:[0,1,1]
	v_pk_fma_f32 v[34:35], v[134:135], v[98:99], v[34:35] op_sel_hi:[0,1,1]
	v_pk_fma_f32 v[32:33], v[134:135], v[106:107], v[32:33] op_sel_hi:[0,1,1]
	v_pk_fma_f32 v[30:31], v[134:135], v[114:115], v[30:31] op_sel_hi:[0,1,1]
	v_pk_fma_f32 v[28:29], v[134:135], v[122:123], v[28:29] op_sel_hi:[0,1,1]
	v_pk_fma_f32 v[0:1], v[224:225], v[72:73], v[0:1] op_sel_hi:[0,1,1]
	v_pk_fma_f32 v[2:3], v[224:225], v[80:81], v[2:3] op_sel_hi:[0,1,1]
	v_pk_fma_f32 v[38:39], v[224:225], v[88:89], v[38:39] op_sel_hi:[0,1,1]
	v_pk_fma_f32 v[36:37], v[224:225], v[96:97], v[36:37] op_sel_hi:[0,1,1]
	v_pk_fma_f32 v[34:35], v[224:225], v[104:105], v[34:35] op_sel_hi:[0,1,1]
	v_pk_fma_f32 v[32:33], v[224:225], v[112:113], v[32:33] op_sel_hi:[0,1,1]
	v_pk_fma_f32 v[30:31], v[224:225], v[120:121], v[30:31] op_sel_hi:[0,1,1]
	v_pk_fma_f32 v[28:29], v[224:225], v[128:129], v[28:29] op_sel_hi:[0,1,1]
	s_waitcnt vmcnt(4)
	v_mov_b32_e32 v130, v168
	v_mov_b32_e32 v132, v170
	v_mov_b32_e32 v134, v172
	v_mov_b32_e32 v224, v174
	s_add_u32 s98, s24, 0x18000
	s_sub_u32 s99, s98, 0xc0000
	s_cmp_ge_u32 s98, 0xc0000
	s_cselect_b32 s98, s99, s98
	s_mov_b32 s99, 0
	v_lshl_add_u64 v[152:153], v[24:25], 0, s[98:99]
	global_load_dword v168, v[152:153], off
	v_add_co_u32_e32 v154, vcc, s64, v152
	s_nop 1
	v_addc_co_u32_e32 v155, vcc, 0, v153, vcc
	global_load_dword v170, v[154:155], off
	v_add_co_u32_e32 v156, vcc, s67, v152
	s_nop 1
	v_addc_co_u32_e32 v157, vcc, 0, v153, vcc
	global_load_dword v172, v[156:157], off
	v_add_co_u32_e32 v158, vcc, s68, v152
	s_nop 1
	v_addc_co_u32_e32 v159, vcc, 0, v153, vcc
	global_load_dword v174, v[158:159], off
	v_mov_b32_e32 v65, s26
	ds_read_b128 v[66:69], v65
	ds_read_b128 v[70:73], v65 offset:256
	ds_read_b128 v[74:77], v65 offset:512
	ds_read_b128 v[78:81], v65 offset:768
	ds_read_b128 v[82:85], v65 offset:1024
	ds_read_b128 v[86:89], v65 offset:1280
	ds_read_b128 v[90:93], v65 offset:1536
	ds_read_b128 v[94:97], v65 offset:1792
	ds_read_b128 v[98:101], v65 offset:2048
	ds_read_b128 v[102:105], v65 offset:2304
	ds_read_b128 v[106:109], v65 offset:2560
	ds_read_b128 v[110:113], v65 offset:2816
	ds_read_b128 v[114:117], v65 offset:3072
	ds_read_b128 v[118:121], v65 offset:3328
	ds_read_b128 v[122:125], v65 offset:3584
	ds_read_b128 v[126:129], v65 offset:3840
	s_waitcnt lgkmcnt(14)
	v_mov_b32_e32 v136, v66
	v_mov_b32_e32 v137, v70
	s_waitcnt lgkmcnt(13)
	v_mov_b32_e32 v138, v74
	s_waitcnt lgkmcnt(12)
	v_mov_b32_e32 v139, v78
	s_waitcnt lgkmcnt(11)
	v_mov_b32_e32 v140, v82
	s_waitcnt lgkmcnt(10)
	v_mov_b32_e32 v141, v86
	s_waitcnt lgkmcnt(9)
	v_mov_b32_e32 v142, v90
	s_waitcnt lgkmcnt(8)
	v_mov_b32_e32 v143, v94
	s_waitcnt lgkmcnt(7)
	v_mov_b32_e32 v144, v98
	s_waitcnt lgkmcnt(6)
	v_mov_b32_e32 v145, v102
	s_waitcnt lgkmcnt(5)
	v_mov_b32_e32 v146, v106
	s_waitcnt lgkmcnt(4)
	v_mov_b32_e32 v147, v110
	s_waitcnt lgkmcnt(3)
	v_mov_b32_e32 v148, v114
	s_waitcnt lgkmcnt(2)
	v_mov_b32_e32 v149, v118
	s_waitcnt lgkmcnt(1)
	v_mov_b32_e32 v150, v122
	s_waitcnt lgkmcnt(0)
	v_mov_b32_e32 v151, v126
	s_add_i32 s26, s26, 16
	v_mov_b32_e32 v70, v67
	v_mov_b32_e32 v78, v75
	v_mov_b32_e32 v86, v83
	v_mov_b32_e32 v94, v91
	v_mov_b32_e32 v102, v99
	v_mov_b32_e32 v110, v107
	v_mov_b32_e32 v118, v115
	v_mov_b32_e32 v126, v123
	s_add_u32 s24, s24, 0xc000
	v_mov_b32_e32 v66, v68
	v_mov_b32_e32 v67, v72
	v_mov_b32_e32 v74, v76
	v_mov_b32_e32 v75, v80
	v_mov_b32_e32 v82, v84
	v_mov_b32_e32 v83, v88
	v_mov_b32_e32 v90, v92
	v_mov_b32_e32 v91, v96
	v_mov_b32_e32 v98, v100
	v_mov_b32_e32 v99, v104
	v_mov_b32_e32 v106, v108
	v_mov_b32_e32 v107, v112
	v_mov_b32_e32 v114, v116
	v_mov_b32_e32 v115, v120
	v_mov_b32_e32 v122, v124
	v_mov_b32_e32 v123, v128
	s_addc_u32 s25, s25, 0
	v_mov_b32_e32 v72, v69
	v_mov_b32_e32 v80, v77
	v_mov_b32_e32 v88, v85
	v_mov_b32_e32 v96, v93
	v_mov_b32_e32 v104, v101
	v_mov_b32_e32 v112, v109
	v_mov_b32_e32 v120, v117
	v_mov_b32_e32 v128, v125
	s_cmp_eq_u32 s24, 0xc0000
	v_pk_fma_f32 v[0:1], v[130:131], v[136:137], v[0:1] op_sel_hi:[0,1,1]
	v_pk_fma_f32 v[2:3], v[130:131], v[138:139], v[2:3] op_sel_hi:[0,1,1]
	v_pk_fma_f32 v[38:39], v[130:131], v[140:141], v[38:39] op_sel_hi:[0,1,1]
	v_pk_fma_f32 v[36:37], v[130:131], v[142:143], v[36:37] op_sel_hi:[0,1,1]
	v_pk_fma_f32 v[34:35], v[130:131], v[144:145], v[34:35] op_sel_hi:[0,1,1]
	v_pk_fma_f32 v[32:33], v[130:131], v[146:147], v[32:33] op_sel_hi:[0,1,1]
	v_pk_fma_f32 v[30:31], v[130:131], v[148:149], v[30:31] op_sel_hi:[0,1,1]
	v_pk_fma_f32 v[28:29], v[130:131], v[150:151], v[28:29] op_sel_hi:[0,1,1]
	v_pk_fma_f32 v[0:1], v[132:133], v[70:71], v[0:1] op_sel_hi:[0,1,1]
	v_pk_fma_f32 v[2:3], v[132:133], v[78:79], v[2:3] op_sel_hi:[0,1,1]
	v_pk_fma_f32 v[38:39], v[132:133], v[86:87], v[38:39] op_sel_hi:[0,1,1]
	v_pk_fma_f32 v[36:37], v[132:133], v[94:95], v[36:37] op_sel_hi:[0,1,1]
	v_pk_fma_f32 v[34:35], v[132:133], v[102:103], v[34:35] op_sel_hi:[0,1,1]
	v_pk_fma_f32 v[32:33], v[132:133], v[110:111], v[32:33] op_sel_hi:[0,1,1]
	v_pk_fma_f32 v[30:31], v[132:133], v[118:119], v[30:31] op_sel_hi:[0,1,1]
	v_pk_fma_f32 v[28:29], v[132:133], v[126:127], v[28:29] op_sel_hi:[0,1,1]
	v_pk_fma_f32 v[0:1], v[134:135], v[66:67], v[0:1] op_sel_hi:[0,1,1]
	v_pk_fma_f32 v[2:3], v[134:135], v[74:75], v[2:3] op_sel_hi:[0,1,1]
	v_pk_fma_f32 v[38:39], v[134:135], v[82:83], v[38:39] op_sel_hi:[0,1,1]
	v_pk_fma_f32 v[36:37], v[134:135], v[90:91], v[36:37] op_sel_hi:[0,1,1]
	v_pk_fma_f32 v[34:35], v[134:135], v[98:99], v[34:35] op_sel_hi:[0,1,1]
	v_pk_fma_f32 v[32:33], v[134:135], v[106:107], v[32:33] op_sel_hi:[0,1,1]
	v_pk_fma_f32 v[30:31], v[134:135], v[114:115], v[30:31] op_sel_hi:[0,1,1]
	v_pk_fma_f32 v[28:29], v[134:135], v[122:123], v[28:29] op_sel_hi:[0,1,1]
	v_pk_fma_f32 v[0:1], v[224:225], v[72:73], v[0:1] op_sel_hi:[0,1,1]
	v_pk_fma_f32 v[2:3], v[224:225], v[80:81], v[2:3] op_sel_hi:[0,1,1]
	v_pk_fma_f32 v[38:39], v[224:225], v[88:89], v[38:39] op_sel_hi:[0,1,1]
	v_pk_fma_f32 v[36:37], v[224:225], v[96:97], v[36:37] op_sel_hi:[0,1,1]
	v_pk_fma_f32 v[34:35], v[224:225], v[104:105], v[34:35] op_sel_hi:[0,1,1]
	v_pk_fma_f32 v[32:33], v[224:225], v[112:113], v[32:33] op_sel_hi:[0,1,1]
	v_pk_fma_f32 v[30:31], v[224:225], v[120:121], v[30:31] op_sel_hi:[0,1,1]
	v_pk_fma_f32 v[28:29], v[224:225], v[128:129], v[28:29] op_sel_hi:[0,1,1]
	s_cbranch_scc0 .LBB0_129
	v_mul_hi_i32 v40, v26, s69
	v_lshrrev_b32_e32 v41, 31, v40
	v_lshrrev_b32_e32 v40, 7, v40
	v_add_u32_e32 v40, v40, v41
	v_mul_lo_u32 v40, v40, s72
	v_sub_u32_e32 v40, v26, v40
	v_cvt_f32_i32_e32 v40, v40
	v_lshl_add_u64 v[24:25], v[24:25], 0, s[20:21]
	v_div_scale_f32 v41, s[24:25], s73, s73, v40
	v_rcp_f32_e32 v65, v41
	v_div_scale_f32 v66, vcc, v40, s73, v40
	v_fma_f32 v67, -v41, v65, 1.0
	v_fmac_f32_e32 v65, v67, v65
	v_mul_f32_e32 v67, v66, v65
	v_fma_f32 v68, -v41, v67, v66
	v_fmac_f32_e32 v67, v68, v65
	v_fma_f32 v41, -v41, v67, v66
	v_div_fmas_f32 v41, v41, v65, v67
	v_div_fixup_f32 v40, v41, s73, v40
	v_fmamk_f32 v65, v40, 0x41447cbd, v43
	v_mul_f32_e64 v40, v6, |v65|
	v_mul_f32_e32 v41, 0x3fb8aa3b, v40
	v_fma_f32 v66, v40, s76, -v41
	v_rndne_f32_e32 v67, v41
	v_fmac_f32_e32 v66, 0x32a5705f, v40
	v_sub_f32_e32 v41, v41, v67
	v_add_f32_e32 v41, v41, v66
	v_cvt_i32_f32_e32 v66, v67
	v_exp_f32_e32 v41, v41
	v_mul_f32_e64 v67, v50, |v65|
	v_cmp_ngt_f32_e32 vcc, s77, v40
	v_ldexp_f32 v41, v41, v66
	v_mul_f32_e32 v66, 0x3fb8aa3b, v67
	v_fma_f32 v68, v67, s76, -v66
	v_rndne_f32_e32 v69, v66
	v_fmac_f32_e32 v68, 0x32a5705f, v67
	v_sub_f32_e32 v66, v66, v69
	v_add_f32_e32 v66, v66, v68
	v_exp_f32_e32 v66, v66
	v_cvt_i32_f32_e32 v68, v69
	v_cndmask_b32_e32 v41, 0, v41, vcc
	v_cmp_nlt_f32_e32 vcc, s78, v40
	s_nop 1
	v_cndmask_b32_e32 v40, v49, v41, vcc
	v_ldexp_f32 v41, v66, v68
	v_mul_f32_e64 v66, v51, |v65|
	v_mul_f32_e32 v68, 0x3fb8aa3b, v66
	v_fma_f32 v69, v66, s76, -v68
	v_rndne_f32_e32 v70, v68
	v_fmac_f32_e32 v69, 0x32a5705f, v66
	v_sub_f32_e32 v68, v68, v70
	v_cmp_ngt_f32_e32 vcc, s77, v67
	v_add_f32_e32 v68, v68, v69
	v_exp_f32_e32 v68, v68
	v_cndmask_b32_e32 v41, 0, v41, vcc
	v_cvt_i32_f32_e32 v69, v70
	v_cmp_nlt_f32_e32 vcc, s78, v67
	s_nop 1
	v_cndmask_b32_e32 v41, v49, v41, vcc
	v_pk_mul_f32 v[0:1], v[40:41], v[0:1]
	v_mul_f32_e64 v41, v52, |v65|
	v_mul_f32_e32 v67, 0x3fb8aa3b, v41
	v_ldexp_f32 v40, v68, v69
	v_fma_f32 v68, v41, s76, -v67
	v_rndne_f32_e32 v69, v67
	v_fmac_f32_e32 v68, 0x32a5705f, v41
	v_sub_f32_e32 v67, v67, v69
	v_add_f32_e32 v67, v67, v68
	v_exp_f32_e32 v67, v67
	v_cvt_i32_f32_e32 v68, v69
	v_cmp_ngt_f32_e32 vcc, s77, v66
	s_nop 1
	v_cndmask_b32_e32 v40, 0, v40, vcc
	v_cmp_nlt_f32_e32 vcc, s78, v66
	v_ldexp_f32 v66, v67, v68
	v_mul_f32_e64 v67, v53, |v65|
	v_mul_f32_e32 v68, 0x3fb8aa3b, v67
	v_fma_f32 v69, v67, s76, -v68
	v_rndne_f32_e32 v70, v68
	v_fmac_f32_e32 v69, 0x32a5705f, v67
	v_sub_f32_e32 v68, v68, v70
	v_cndmask_b32_e32 v40, v49, v40, vcc
	v_cmp_ngt_f32_e32 vcc, s77, v41
	v_add_f32_e32 v68, v68, v69
	v_exp_f32_e32 v68, v68
	v_cndmask_b32_e32 v66, 0, v66, vcc
	v_cvt_i32_f32_e32 v69, v70
	v_cmp_nlt_f32_e32 vcc, s78, v41
	s_nop 1
	v_cndmask_b32_e32 v41, v49, v66, vcc
	v_pk_mul_f32 v[2:3], v[40:41], v[2:3]
	v_mul_f32_e64 v41, v54, |v65|
	v_mul_f32_e32 v66, 0x3fb8aa3b, v41
	v_ldexp_f32 v40, v68, v69
	v_fma_f32 v68, v41, s76, -v66
	v_rndne_f32_e32 v69, v66
	v_fmac_f32_e32 v68, 0x32a5705f, v41
	v_sub_f32_e32 v66, v66, v69
	v_add_f32_e32 v66, v66, v68
	v_exp_f32_e32 v66, v66
	v_cvt_i32_f32_e32 v68, v69
	v_cmp_ngt_f32_e32 vcc, s77, v67
	v_ldexp_f32 v66, v66, v68
	s_nop 0
	v_cndmask_b32_e32 v40, 0, v40, vcc
	v_cmp_nlt_f32_e32 vcc, s78, v67
	v_mul_f32_e64 v67, v55, |v65|
	v_mul_f32_e32 v68, 0x3fb8aa3b, v67
	v_fma_f32 v69, v67, s76, -v68
	v_rndne_f32_e32 v70, v68
	v_fmac_f32_e32 v69, 0x32a5705f, v67
	v_sub_f32_e32 v68, v68, v70
	v_cndmask_b32_e32 v40, v49, v40, vcc
	v_cmp_ngt_f32_e32 vcc, s77, v41
	v_add_f32_e32 v68, v68, v69
	v_exp_f32_e32 v68, v68
	v_cndmask_b32_e32 v66, 0, v66, vcc
	v_cvt_i32_f32_e32 v69, v70
	v_cmp_nlt_f32_e32 vcc, s78, v41
	s_nop 1
	v_cndmask_b32_e32 v41, v49, v66, vcc
	v_pk_mul_f32 v[38:39], v[40:41], v[38:39]
	v_mul_f32_e64 v41, v56, |v65|
	v_mul_f32_e32 v66, 0x3fb8aa3b, v41
	v_ldexp_f32 v40, v68, v69
	v_fma_f32 v68, v41, s76, -v66
	v_rndne_f32_e32 v69, v66
	v_fmac_f32_e32 v68, 0x32a5705f, v41
	v_sub_f32_e32 v66, v66, v69
	v_add_f32_e32 v66, v66, v68
	v_exp_f32_e32 v66, v66
	v_cvt_i32_f32_e32 v68, v69
	v_cmp_ngt_f32_e32 vcc, s77, v67
	v_ldexp_f32 v66, v66, v68
	s_nop 0
	v_cndmask_b32_e32 v40, 0, v40, vcc
	v_cmp_nlt_f32_e32 vcc, s78, v67
	v_mul_f32_e64 v67, v57, |v65|
	v_mul_f32_e32 v68, 0x3fb8aa3b, v67
	v_fma_f32 v69, v67, s76, -v68
	v_rndne_f32_e32 v70, v68
	v_fmac_f32_e32 v69, 0x32a5705f, v67
	v_sub_f32_e32 v68, v68, v70
	v_cndmask_b32_e32 v40, v49, v40, vcc
	v_cmp_ngt_f32_e32 vcc, s77, v41
	v_add_f32_e32 v68, v68, v69
	v_exp_f32_e32 v68, v68
	v_cndmask_b32_e32 v66, 0, v66, vcc
	v_cvt_i32_f32_e32 v69, v70
	v_cmp_nlt_f32_e32 vcc, s78, v41
	s_nop 1
	v_cndmask_b32_e32 v41, v49, v66, vcc
	v_pk_mul_f32 v[40:41], v[40:41], v[36:37]
	v_mul_f32_e64 v37, v58, |v65|
	v_mul_f32_e32 v66, 0x3fb8aa3b, v37
	v_ldexp_f32 v36, v68, v69
	v_fma_f32 v68, v37, s76, -v66
	v_rndne_f32_e32 v69, v66
	v_fmac_f32_e32 v68, 0x32a5705f, v37
	v_sub_f32_e32 v66, v66, v69
	v_add_f32_e32 v66, v66, v68
	v_exp_f32_e32 v66, v66
	v_cvt_i32_f32_e32 v68, v69
	v_cmp_ngt_f32_e32 vcc, s77, v67
	v_ldexp_f32 v66, v66, v68
	s_nop 0
	v_cndmask_b32_e32 v36, 0, v36, vcc
	v_cmp_nlt_f32_e32 vcc, s78, v67
	v_mul_f32_e64 v67, v59, |v65|
	v_mul_f32_e32 v68, 0x3fb8aa3b, v67
	v_fma_f32 v69, v67, s76, -v68
	v_rndne_f32_e32 v70, v68
	v_fmac_f32_e32 v69, 0x32a5705f, v67
	v_sub_f32_e32 v68, v68, v70
	v_cndmask_b32_e32 v36, v49, v36, vcc
	v_cmp_ngt_f32_e32 vcc, s77, v37
	v_add_f32_e32 v68, v68, v69
	v_exp_f32_e32 v68, v68
	v_cndmask_b32_e32 v66, 0, v66, vcc
	v_cvt_i32_f32_e32 v69, v70
	v_cmp_nlt_f32_e32 vcc, s78, v37
	s_nop 1
	v_cndmask_b32_e32 v37, v49, v66, vcc
	v_pk_mul_f32 v[34:35], v[36:37], v[34:35]
	v_mul_f32_e64 v37, v60, |v65|
	v_mul_f32_e32 v66, 0x3fb8aa3b, v37
	v_ldexp_f32 v36, v68, v69
	v_fma_f32 v68, v37, s76, -v66
	v_rndne_f32_e32 v69, v66
	v_fmac_f32_e32 v68, 0x32a5705f, v37
	v_sub_f32_e32 v66, v66, v69
	v_add_f32_e32 v66, v66, v68
	v_exp_f32_e32 v66, v66
	v_cvt_i32_f32_e32 v68, v69
	v_cmp_ngt_f32_e32 vcc, s77, v67
	v_ldexp_f32 v66, v66, v68
	s_nop 0
	v_cndmask_b32_e32 v36, 0, v36, vcc
	v_cmp_nlt_f32_e32 vcc, s78, v67
	v_mul_f32_e64 v67, v61, |v65|
	v_mul_f32_e32 v68, 0x3fb8aa3b, v67
	v_fma_f32 v69, v67, s76, -v68
	v_rndne_f32_e32 v70, v68
	v_fmac_f32_e32 v69, 0x32a5705f, v67
	v_sub_f32_e32 v68, v68, v70
	v_cndmask_b32_e32 v36, v49, v36, vcc
	v_cmp_ngt_f32_e32 vcc, s77, v37
	v_add_f32_e32 v68, v68, v69
	v_exp_f32_e32 v68, v68
	v_cndmask_b32_e32 v66, 0, v66, vcc
	v_cvt_i32_f32_e32 v69, v70
	v_cmp_nlt_f32_e32 vcc, s78, v37
	s_nop 1
	v_cndmask_b32_e32 v37, v49, v66, vcc
	v_pk_mul_f32 v[36:37], v[36:37], v[32:33]
	v_mul_f32_e64 v33, v62, |v65|
	v_mul_f32_e32 v66, 0x3fb8aa3b, v33
	v_ldexp_f32 v32, v68, v69
	v_fma_f32 v68, v33, s76, -v66
	v_rndne_f32_e32 v69, v66
	v_fmac_f32_e32 v68, 0x32a5705f, v33
	v_sub_f32_e32 v66, v66, v69
	v_add_f32_e32 v66, v66, v68
	v_exp_f32_e32 v66, v66
	v_cvt_i32_f32_e32 v68, v69
	v_cmp_ngt_f32_e32 vcc, s77, v67
	v_ldexp_f32 v66, v66, v68
	s_nop 0
	v_cndmask_b32_e32 v32, 0, v32, vcc
	v_cmp_nlt_f32_e32 vcc, s78, v67
	v_mul_f32_e64 v67, v63, |v65|
	v_mul_f32_e32 v68, 0x3fb8aa3b, v67
	v_fma_f32 v69, v67, s76, -v68
	v_rndne_f32_e32 v70, v68
	v_fmac_f32_e32 v69, 0x32a5705f, v67
	v_sub_f32_e32 v68, v68, v70
	v_cndmask_b32_e32 v32, v49, v32, vcc
	v_cmp_ngt_f32_e32 vcc, s77, v33
	v_add_f32_e32 v68, v68, v69
	v_exp_f32_e32 v68, v68
	v_cndmask_b32_e32 v66, 0, v66, vcc
	v_cvt_i32_f32_e32 v69, v70
	v_cmp_nlt_f32_e32 vcc, s78, v33
	s_nop 1
	v_cndmask_b32_e32 v33, v49, v66, vcc
	v_pk_mul_f32 v[30:31], v[32:33], v[30:31]
	v_mul_f32_e64 v33, v64, |v65|
	v_mul_f32_e32 v65, 0x3fb8aa3b, v33
	v_ldexp_f32 v32, v68, v69
	v_fma_f32 v66, v33, s76, -v65
	v_rndne_f32_e32 v68, v65
	v_fmac_f32_e32 v66, 0x32a5705f, v33
	v_sub_f32_e32 v65, v65, v68
	v_add_f32_e32 v65, v65, v66
	v_exp_f32_e32 v65, v65
	v_cvt_i32_f32_e32 v66, v68
	v_cmp_ngt_f32_e32 vcc, s77, v67
	v_ldexp_f32 v65, v65, v66
	s_nop 0
	v_cndmask_b32_e32 v32, 0, v32, vcc
	v_cmp_nlt_f32_e32 vcc, s78, v67
	s_nop 1
	v_cndmask_b32_e32 v32, v49, v32, vcc
	v_cmp_ngt_f32_e32 vcc, s77, v33
	s_nop 1
	v_cndmask_b32_e32 v65, 0, v65, vcc
	v_cmp_nlt_f32_e32 vcc, s78, v33
	s_nop 1
	v_cndmask_b32_e32 v33, v49, v65, vcc
	v_pk_mul_f32 v[32:33], v[32:33], v[28:29]
	v_lshlrev_b64 v[28:29], 14, v[26:27]
	v_lshl_add_u64 v[28:29], s[10:11], 0, v[28:29]
	global_store_dwordx4 v[28:29], v[0:3], off
	global_store_dwordx4 v[28:29], v[38:41], off offset:16
	global_store_dwordx4 v[28:29], v[34:37], off offset:32
	global_store_dwordx4 v[28:29], v[30:33], off offset:48
	v_add_f32_e64 v0, |v0|, |v1|
	v_add_f32_e64 v0, v0, |v2|
	v_add_f32_e64 v0, v0, |v3|
	v_add_f32_e64 v0, v0, |v38|
	v_add_f32_e64 v0, v0, |v39|
	v_add_f32_e64 v0, v0, |v40|
	v_add_f32_e64 v0, v0, |v41|
	v_add_f32_e64 v0, v0, |v34|
	v_add_f32_e64 v0, v0, |v35|
	v_add_f32_e64 v0, v0, |v36|
	v_add_f32_e64 v0, v0, |v37|
	v_add_f32_e64 v0, v0, |v30|
	v_add_f32_e64 v0, v0, |v31|
	v_add_f32_e64 v0, v0, |v32|
	v_add_f32_e64 v2, v0, |v33|
	v_lshl_add_u64 v[0:1], v[26:27], 2, s[12:13]
	global_store_dword v[0:1], v2, off
	v_add_u32_e32 v0, 0x200, v26
	v_cmp_lt_i32_e32 vcc, s79, v26
	s_or_b64 s[22:23], vcc, s[22:23]
	v_mov_b32_e32 v26, v0
	s_andn2_b64 exec, exec, s[22:23]
	s_cbranch_execnz .LBB0_128
	s_branch .LBB0_79

.LBB0_538:
	s_or_b64 exec, exec, s[4:5]
	v_add_u32_e32 v0, -7, v17
	v_ldexp_f32 v184, 1.0, v0
	s_waitcnt lgkmcnt(0)
	v_alignbyte_b32 v14, v11, v10, 1
	v_alignbyte_b32 v15, v6, v11, 1
	v_alignbyte_b32 v31, v7, v6, 1
	v_mov_b32_e32 v4, v10
	v_mov_b32_e32 v5, v11
	v_add_u32_e32 v0, 0x10890, v193
	v_alignbyte_b32 v12, v9, v8, 1
	v_alignbyte_b32 v13, v10, v9, 1
	v_alignbyte_b32 v16, v9, v8, 2
	v_alignbyte_b32 v17, v10, v9, 2
	v_alignbyte_b32 v18, v11, v10, 2
	v_alignbyte_b32 v19, v6, v11, 2
	v_alignbyte_b32 v20, v9, v8, 3
	v_alignbyte_b32 v21, v10, v9, 3
	v_alignbyte_b32 v22, v11, v10, 3
	v_alignbyte_b32 v23, v6, v11, 3
	v_pk_mov_b32 v[24:25], v[8:9], v[10:11] op_sel:[1,0]
	v_pk_mov_b32 v[26:27], v[10:11], v[6:7] op_sel:[1,0]
	v_alignbyte_b32 v35, v7, v6, 2
	ds_write_b128 v0, v[4:7]
	v_alignbyte_b32 v11, v2, v7, 1
	v_mov_b32_e32 v8, v14
	v_mov_b32_e32 v9, v15
	v_mov_b32_e32 v10, v31
	v_add_u32_e32 v0, 0x129b0, v193
	v_alignbyte_b32 v39, v7, v6, 3
	ds_write_b128 v0, v[8:11]
	v_alignbyte_b32 v45, v2, v7, 2
	v_mov_b32_e32 v42, v18
	v_mov_b32_e32 v43, v19
	v_mov_b32_e32 v44, v35
	v_add_u32_e32 v0, 0x14ad0, v193
	ds_write_b128 v0, v[42:45]
	v_alignbyte_b32 v49, v2, v7, 3
	v_mov_b32_e32 v46, v22
	v_mov_b32_e32 v47, v23
	v_mov_b32_e32 v48, v39
	v_add_u32_e32 v0, 0x16bf0, v193
	ds_write_b128 v0, v[46:49]
	v_pk_mov_b32 v[6:7], v[6:7], v[2:3] op_sel:[1,0]
	v_mov_b32_e32 v4, v26
	v_mov_b32_e32 v5, v27
	v_add_u32_e32 v0, 0x18c80, v193
	ds_write_b128 v0, v[4:7]
	v_alignbyte_b32 v7, v3, v2, 1
	v_mov_b32_e32 v4, v15
	v_mov_b32_e32 v5, v31
	v_mov_b32_e32 v6, v11
	v_add_u32_e32 v0, 0x1ada0, v193
	ds_write_b128 v0, v[4:7]
	v_alignbyte_b32 v7, v3, v2, 2
	v_mov_b32_e32 v4, v19
	v_mov_b32_e32 v5, v35
	v_mov_b32_e32 v6, v45
	v_add_u32_e32 v0, 0x1cec0, v193
	ds_write_b128 v0, v[4:7]
	v_alignbyte_b32 v3, v3, v2, 3
	v_mov_b32_e32 v0, v23
	v_mov_b32_e32 v1, v39
	v_mov_b32_e32 v2, v49
	v_add_u32_e32 v4, 0x1efe0, v193
	ds_write_b128 v4, v[0:3]
	v_lshl_add_u64 v[0:1], s[36:37], 0, v[178:179]
	v_lshlrev_b64 v[186:187], 12, v[0:1]
	v_mov_b32_e32 v28, v13
	v_mov_b32_e32 v29, v14
	v_mov_b32_e32 v30, v15
	v_mov_b32_e32 v32, v17
	v_mov_b32_e32 v33, v18
	v_mov_b32_e32 v34, v19
	v_mov_b32_e32 v36, v21
	v_mov_b32_e32 v37, v22
	v_mov_b32_e32 v38, v23
	v_lshl_add_u64 v[188:189], v[180:181], 0, v[186:187]
	ds_write_b128 v193, v[12:15] offset:8480
	ds_write_b128 v193, v[16:19] offset:16960
	ds_write_b128 v193, v[20:23] offset:25440
	ds_write_b128 v193, v[24:27] offset:33808
	ds_write_b128 v193, v[28:31] offset:42288
	ds_write_b128 v193, v[32:35] offset:50768
	ds_write_b128 v193, v[36:39] offset:59248
	s_waitcnt lgkmcnt(0)
	s_barrier
	global_load_dwordx4 v[0:3], v[188:189], off
	global_load_dwordx4 v[4:7], v[188:189], off offset:16
	ds_read_b128 v[8:11], v192 offset:416
	ds_read_b128 v[12:15], v192 offset:432
	ds_read_b128 v[16:19], v192 offset:448
	ds_read_b128 v[20:23], v192 offset:464
	ds_read_b128 v[24:27], v192 offset:480
	ds_read_b128 v[28:31], v192 offset:496
	ds_read_b128 v[32:35], v192 offset:512
	s_mov_b32 s4, 0
	v_mov_b32_e32 v41, v40
	v_mov_b32_e32 v42, v40
	v_mov_b32_e32 v43, v40
	v_mov_b32_e32 v44, v40
	v_mov_b32_e32 v45, v40
	v_mov_b32_e32 v46, v40
	v_mov_b32_e32 v47, v40
	v_mov_b32_e32 v48, v40
	v_mov_b32_e32 v49, v40
	v_mov_b32_e32 v50, v40
	v_mov_b32_e32 v51, v40
	v_mov_b32_e32 v52, v40
	v_mov_b32_e32 v53, v40
	v_mov_b32_e32 v54, v40
	v_mov_b32_e32 v55, v40
	v_mov_b32_e32 v56, v40
	v_mov_b32_e32 v57, v40
	v_mov_b32_e32 v58, v40
	v_mov_b32_e32 v59, v40
	v_mov_b32_e32 v60, v40
	v_mov_b32_e32 v61, v40
	v_mov_b32_e32 v62, v40
	v_mov_b32_e32 v63, v40
	v_mov_b32_e32 v64, v40
	v_mov_b32_e32 v65, v40
	v_mov_b32_e32 v66, v40
	v_mov_b32_e32 v67, v40
	v_mov_b32_e32 v68, v40
	v_mov_b32_e32 v69, v40
	v_mov_b32_e32 v70, v40
	v_mov_b32_e32 v71, v40
	v_mov_b32_e32 v72, v40
	v_mov_b32_e32 v73, v40
	v_mov_b32_e32 v74, v40
	v_mov_b32_e32 v75, v40
	v_mov_b32_e32 v76, v40
	v_mov_b32_e32 v77, v40
	v_mov_b32_e32 v78, v40
	v_mov_b32_e32 v79, v40
	v_mov_b32_e32 v80, v40
	v_mov_b32_e32 v81, v40
	v_mov_b32_e32 v82, v40
	v_mov_b32_e32 v83, v40
	v_mov_b32_e32 v84, v40
	v_mov_b32_e32 v85, v40
	v_mov_b32_e32 v86, v40
	v_mov_b32_e32 v87, v40
	v_mov_b32_e32 v88, v40
	v_mov_b32_e32 v89, v40
	v_mov_b32_e32 v90, v40
	v_mov_b32_e32 v91, v40
	v_mov_b32_e32 v92, v40
	v_mov_b32_e32 v93, v40
	v_mov_b32_e32 v94, v40
	v_mov_b32_e32 v95, v40
	v_mov_b32_e32 v96, v40
	v_mov_b32_e32 v97, v40
	v_mov_b32_e32 v98, v40
	v_mov_b32_e32 v99, v40
	v_mov_b32_e32 v100, v40
	v_mov_b32_e32 v101, v40
	v_mov_b32_e32 v102, v40
	v_mov_b32_e32 v103, v40
	v_mov_b32_e32 v104, v40
	v_mov_b32_e32 v105, v40
	v_mov_b32_e32 v106, v40
	v_mov_b32_e32 v107, v40
	v_mov_b32_e32 v108, v40
	v_mov_b32_e32 v109, v40
	v_mov_b32_e32 v110, v40
	v_mov_b32_e32 v111, v40
	v_mov_b32_e32 v112, v40
	v_mov_b32_e32 v113, v40
	v_mov_b32_e32 v114, v40
	v_mov_b32_e32 v115, v40
	v_mov_b32_e32 v116, v40
	v_mov_b32_e32 v117, v40
	v_mov_b32_e32 v118, v40
	v_mov_b32_e32 v119, v40
	v_mov_b32_e32 v120, v40
	v_mov_b32_e32 v121, v40
	v_mov_b32_e32 v122, v40
	v_mov_b32_e32 v123, v40
	v_mov_b32_e32 v124, v40
	v_mov_b32_e32 v125, v40
	v_mov_b32_e32 v126, v40
	v_mov_b32_e32 v127, v40
	v_mov_b32_e32 v128, v40
	v_mov_b32_e32 v129, v40
	v_mov_b32_e32 v130, v40
	v_mov_b32_e32 v131, v40
	v_mov_b32_e32 v132, v40
	v_mov_b32_e32 v133, v40
	v_mov_b32_e32 v134, v40
	v_mov_b32_e32 v135, v40
	v_mov_b32_e32 v136, v40
	v_mov_b32_e32 v137, v40
	v_mov_b32_e32 v138, v40
	v_mov_b32_e32 v139, v40
	v_mov_b32_e32 v140, v40
	v_mov_b32_e32 v141, v40
	v_mov_b32_e32 v142, v40
	v_mov_b32_e32 v143, v40
	v_mov_b32_e32 v144, v40
	v_mov_b32_e32 v145, v40
	v_mov_b32_e32 v146, v40
	v_mov_b32_e32 v147, v40
	v_mov_b32_e32 v148, v40
	v_mov_b32_e32 v149, v40
	v_mov_b32_e32 v150, v40
	v_mov_b32_e32 v151, v40
	v_mov_b32_e32 v152, v40
	v_mov_b32_e32 v153, v40
	v_mov_b32_e32 v154, v40
	v_mov_b32_e32 v155, v40
	v_mov_b32_e32 v156, v40
	v_mov_b32_e32 v157, v40
	v_mov_b32_e32 v158, v40
	v_mov_b32_e32 v159, v40
	v_mov_b32_e32 v160, v40
	v_mov_b32_e32 v161, v40
	v_mov_b32_e32 v162, v40
	v_mov_b32_e32 v163, v40
	v_mov_b32_e32 v164, v40
	v_mov_b32_e32 v165, v40
	v_mov_b32_e32 v166, v40
	v_mov_b32_e32 v167, v40
.LBB0_539:
	s_add_i32 s5, s4, 0x80
	s_and_b32 s72, s5, 0xf80
	v_lshl_add_u64 v[168:169], v[188:189], 0, s[72:73]
	global_load_dwordx4 v[172:175], v[168:169], off
	s_nop 0
	global_load_dwordx4 v[168:171], v[168:169], off offset:16
	v_add_u32_e32 v185, s4, v192
	v_add_u32_e32 v203, s72, v192
	ds_read_b128 v[204:207], v185 offset:320
	ds_read_b128 v[208:211], v185 offset:336
	ds_read_b128 v[212:215], v185 offset:352
	ds_read_b128 v[216:219], v185 offset:368
	ds_read_b128 v[220:223], v185 offset:384
	ds_read_b128 v[224:227], v185 offset:400
	ds_read_b128 v[228:231], v185 offset:416
	s_waitcnt vmcnt(2) lgkmcnt(7)
	v_mfma_f32_16x16x128_f8f6f4 v[164:167], v[28:35], v[0:7], v[164:167]
	v_mfma_f32_16x16x128_f8f6f4 v[160:163], v[24:31], v[0:7], v[160:163]
	v_mfma_f32_16x16x128_f8f6f4 v[156:159], v[20:27], v[0:7], v[156:159]
	v_mfma_f32_16x16x128_f8f6f4 v[152:155], v[16:23], v[0:7], v[152:155]
	v_mfma_f32_16x16x128_f8f6f4 v[148:151], v[12:19], v[0:7], v[148:151]
	v_mfma_f32_16x16x128_f8f6f4 v[144:147], v[8:15], v[0:7], v[144:147]
	ds_read_b128 v[8:11], v185 offset:240
	ds_read_b128 v[12:15], v185 offset:256
	ds_read_b128 v[16:19], v185 offset:272
	ds_read_b128 v[20:23], v185 offset:288
	ds_read_b128 v[24:27], v185 offset:304
	ds_read_b128 v[28:31], v185 offset:320
	s_waitcnt lgkmcnt(6)
	v_mfma_f32_16x16x128_f8f6f4 v[140:143], v[224:231], v[0:7], v[140:143]
	v_mfma_f32_16x16x128_f8f6f4 v[136:139], v[220:227], v[0:7], v[136:139]
	v_mfma_f32_16x16x128_f8f6f4 v[132:135], v[216:223], v[0:7], v[132:135]
	v_mfma_f32_16x16x128_f8f6f4 v[128:131], v[212:219], v[0:7], v[128:131]
	v_mfma_f32_16x16x128_f8f6f4 v[124:127], v[208:215], v[0:7], v[124:127]
	v_mfma_f32_16x16x128_f8f6f4 v[120:123], v[204:211], v[0:7], v[120:123]
	ds_read_b128 v[204:207], v185 offset:160
	ds_read_b128 v[208:211], v185 offset:176
	ds_read_b128 v[212:215], v185 offset:192
	ds_read_b128 v[216:219], v185 offset:208
	ds_read_b128 v[220:223], v185 offset:224
	ds_read_b128 v[224:227], v185 offset:240
	s_waitcnt lgkmcnt(6)
	v_mfma_f32_16x16x128_f8f6f4 v[116:119], v[24:31], v[0:7], v[116:119]
	v_mfma_f32_16x16x128_f8f6f4 v[112:115], v[20:27], v[0:7], v[112:115]
	v_mfma_f32_16x16x128_f8f6f4 v[108:111], v[16:23], v[0:7], v[108:111]
	v_mfma_f32_16x16x128_f8f6f4 v[104:107], v[12:19], v[0:7], v[104:107]
	v_mfma_f32_16x16x128_f8f6f4 v[100:103], v[8:15], v[0:7], v[100:103]
	ds_read_b128 v[8:11], v185 offset:80
	ds_read_b128 v[12:15], v185 offset:96
	ds_read_b128 v[16:19], v185 offset:112
	ds_read_b128 v[20:23], v185 offset:128
	ds_read_b128 v[24:27], v185 offset:144
	ds_read_b128 v[28:31], v185 offset:160
	s_waitcnt lgkmcnt(6)
	v_mfma_f32_16x16x128_f8f6f4 v[96:99], v[220:227], v[0:7], v[96:99]
	v_mfma_f32_16x16x128_f8f6f4 v[92:95], v[216:223], v[0:7], v[92:95]
	v_mfma_f32_16x16x128_f8f6f4 v[88:91], v[212:219], v[0:7], v[88:91]
	v_mfma_f32_16x16x128_f8f6f4 v[84:87], v[208:215], v[0:7], v[84:87]
	v_mfma_f32_16x16x128_f8f6f4 v[80:83], v[204:211], v[0:7], v[80:83]
	ds_read_b128 v[204:207], v185 offset:0
	ds_read_b128 v[208:211], v185 offset:16
	ds_read_b128 v[212:215], v185 offset:32
	ds_read_b128 v[216:219], v185 offset:48
	ds_read_b128 v[220:223], v185 offset:64
	ds_read_b128 v[224:227], v185 offset:80
	s_waitcnt lgkmcnt(6)
	v_mfma_f32_16x16x128_f8f6f4 v[76:79], v[24:31], v[0:7], v[76:79]
	v_mfma_f32_16x16x128_f8f6f4 v[72:75], v[20:27], v[0:7], v[72:75]
	v_mfma_f32_16x16x128_f8f6f4 v[68:71], v[16:23], v[0:7], v[68:71]
	v_mfma_f32_16x16x128_f8f6f4 v[64:67], v[12:19], v[0:7], v[64:67]
	v_mfma_f32_16x16x128_f8f6f4 v[60:63], v[8:15], v[0:7], v[60:63]
	ds_read_b128 v[8:11], v203 offset:416
	ds_read_b128 v[12:15], v203 offset:432
	ds_read_b128 v[16:19], v203 offset:448
	ds_read_b128 v[20:23], v203 offset:464
	ds_read_b128 v[24:27], v203 offset:480
	ds_read_b128 v[28:31], v203 offset:496
	ds_read_b128 v[32:35], v203 offset:512
	s_waitcnt lgkmcnt(7)
	v_mfma_f32_16x16x128_f8f6f4 v[56:59], v[220:227], v[0:7], v[56:59]
	v_mfma_f32_16x16x128_f8f6f4 v[52:55], v[216:223], v[0:7], v[52:55]
	v_mfma_f32_16x16x128_f8f6f4 v[48:51], v[212:219], v[0:7], v[48:51]
	v_mfma_f32_16x16x128_f8f6f4 v[44:47], v[208:215], v[0:7], v[44:47]
	v_mfma_f32_16x16x128_f8f6f4 v[40:43], v[204:211], v[0:7], v[40:43]
	s_cmpk_eq_i32 s5, 0x1000
	s_mov_b32 s4, s5
	s_waitcnt vmcnt(0)
	v_mov_b32_e32 v0, v172
	v_mov_b32_e32 v1, v173
	v_mov_b32_e32 v2, v174
	v_mov_b32_e32 v3, v175
	v_mov_b32_e32 v4, v168
	v_mov_b32_e32 v5, v169
	v_mov_b32_e32 v6, v170
	v_mov_b32_e32 v7, v171
	s_cbranch_scc0 .LBB0_539
	s_lshl_b64 s[4:5], s[36:37], 2
	s_add_u32 s4, s31, s4
	s_addc_u32 s5, s46, s5
	global_load_dword v4, v245, s[4:5]
	v_lshl_add_u64 v[0:1], v[186:187], 0, v[182:183]
	v_lshlrev_b64 v[2:3], 1, v[0:1]
	v_lshl_add_u64 v[8:9], s[22:23], 0, v[2:3]
	v_lshl_add_u64 v[6:7], s[24:25], 0, v[2:3]
	global_load_dwordx2 v[168:169], v[8:9], off
	global_load_dwordx2 v[170:171], v[6:7], off
	s_waitcnt lgkmcnt(0)
	global_load_dwordx2 v[36:37], v[8:9], off offset:32
	global_load_dwordx2 v[34:35], v[6:7], off offset:32
	global_load_dwordx2 v[32:33], v[8:9], off offset:64
	global_load_dwordx2 v[30:31], v[6:7], off offset:64
	global_load_dwordx2 v[26:27], v[8:9], off offset:96
	global_load_dwordx2 v[28:29], v[6:7], off offset:96
	global_load_dwordx2 v[24:25], v[8:9], off offset:128
	global_load_dwordx2 v[22:23], v[6:7], off offset:128
	global_load_dwordx2 v[20:21], v[8:9], off offset:160
	global_load_dwordx2 v[18:19], v[6:7], off offset:160
	global_load_dwordx2 v[16:17], v[8:9], off offset:192
	global_load_dwordx2 v[14:15], v[6:7], off offset:192
	global_load_dwordx2 v[10:11], v[8:9], off offset:224
	global_load_dwordx2 v[12:13], v[6:7], off offset:224
	v_mov_b32_e32 v38, v164
	v_mov_b32_e32 v39, v166
	v_mov_b32_e32 v166, v165
	v_lshl_add_u64 v[2:3], s[26:27], 0, v[2:3]
	v_lshl_add_u64 v[0:1], s[28:29], 0, v[0:1]
	s_and_b64 vcc, exec, s[34:35]
	s_waitcnt vmcnt(15)
	v_and_b32_e32 v165, 0xffff0000, v169
	v_and_b32_e32 v164, 0xffff0000, v168
	v_lshlrev_b32_e32 v173, 16, v169
	v_lshlrev_b32_e32 v172, 16, v168
	v_pk_mul_f32 v[164:165], v[4:5], v[164:165] op_sel_hi:[0,1]
	v_pk_mul_f32 v[172:173], v[4:5], v[172:173] op_sel_hi:[0,1]
	v_pk_fma_f32 v[164:165], v[184:185], v[166:167], v[164:165] op_sel_hi:[0,1,1]
	s_waitcnt vmcnt(14)
	v_and_b32_e32 v167, 0xffff0000, v171
	v_and_b32_e32 v166, 0xffff0000, v170
	v_pk_fma_f32 v[38:39], v[184:185], v[38:39], v[172:173] op_sel_hi:[0,1,1]
	v_lshlrev_b32_e32 v173, 16, v171
	v_lshlrev_b32_e32 v172, 16, v170
	v_pk_mul_f32 v[164:165], v[164:165], v[166:167]
	v_pk_mul_f32 v[38:39], v[38:39], v[172:173]
	v_and_b32_sdwa v167, v165, v253 dst_sel:DWORD dst_unused:UNUSED_PAD src0_sel:WORD_1 src1_sel:DWORD
	v_and_b32_sdwa v168, v164, v253 dst_sel:DWORD dst_unused:UNUSED_PAD src0_sel:WORD_1 src1_sel:DWORD
	v_and_b32_sdwa v5, v39, v253 dst_sel:DWORD dst_unused:UNUSED_PAD src0_sel:WORD_1 src1_sel:DWORD
	v_and_b32_sdwa v166, v38, v253 dst_sel:DWORD dst_unused:UNUSED_PAD src0_sel:WORD_1 src1_sel:DWORD
	v_add3_u32 v167, v165, v167, s94
	v_add3_u32 v168, v164, v168, s94
	v_add3_u32 v166, v38, v166, s94
	v_add3_u32 v5, v39, v5, s94
	v_and_b32_e32 v167, 0xffff0000, v167
	v_and_b32_e32 v168, 0xffff0000, v168
	v_or_b32_sdwa v167, v167, v5 dst_sel:DWORD dst_unused:UNUSED_PAD src0_sel:DWORD src1_sel:WORD_1
	v_or_b32_sdwa v166, v168, v166 dst_sel:DWORD dst_unused:UNUSED_PAD src0_sel:DWORD src1_sel:WORD_1
	global_store_dwordx2 v[2:3], v[166:167], off
	s_cbranch_vccz .LBB0_542
	v_max_f32_e32 v5, v38, v38
	v_mov_b32_e32 v166, 0x43dc0000
	v_max_f32_e32 v38, v164, v164
	v_med3_f32 v5, v5, s77, v166
	v_med3_f32 v38, v38, s77, v166
	v_mov_b32_e32 v164, v245
	v_cvt_pk_fp8_f32 v164, v5, v38
	v_max_f32_e32 v5, v39, v39
	v_max_f32_e32 v38, v165, v165
	v_med3_f32 v5, v5, s77, v166
	v_med3_f32 v38, v38, s77, v166
	v_cvt_pk_fp8_f32 v164, v5, v38 op_sel:[0,0,1]
	global_store_dword v[0:1], v164, off

.LBB0_608:
	v_readlane_b32 s0, v254, 52
	s_add_u32 s22, s20, 0x3ba00000
	s_addc_u32 s23, s21, 0
	v_mov_b32_e32 v0, s0
	ds_read_b64 v[0:1], v0
	s_mov_b32 s34, s74
	s_movk_i32 s98, 0x1800
	s_cmp_lg_u32 s70, 0x100
	s_cbranch_scc1 .Lna_map_done
	s_mul_i32 s34, s74, 24
	s_add_i32 s98, s34, 24
.Lna_map_done:
	v_lshrrev_b32_e32 v155, 4, v201
	s_waitcnt vmcnt(0)
	v_add_u32_e32 v79, 0x200, v200
	v_add_u32_e32 v78, 0x400, v200
	s_waitcnt lgkmcnt(0)
	v_readfirstlane_b32 s4, v0
	v_readfirstlane_b32 s5, v1
	s_add_u32 s24, s4, s51
	s_addc_u32 s25, s5, 0
	v_add_u32_e32 v77, 0x600, v200
	v_add_u32_e32 v76, 0x800, v200
	v_add_u32_e32 v75, 0xa00, v200
	v_add_u32_e32 v74, 0xc00, v200
	v_add_u32_e32 v73, 0xe00, v200
	v_add_u32_e32 v84, 0x1000, v200
	s_movk_i32 s0, 0x1d1
	s_cmpk_lt_i32 s34, 0x1800
	v_and_b32_e32 v154, 15, v190
	v_bfe_u32 v156, v200, 3, 6
	v_ashrrev_i32_e32 v157, 9, v200
	v_ashrrev_i32_e32 v158, 9, v79
	v_ashrrev_i32_e32 v159, 9, v78
	v_ashrrev_i32_e32 v160, 9, v77
	v_ashrrev_i32_e32 v161, 9, v76
	v_ashrrev_i32_e32 v162, 9, v75
	v_ashrrev_i32_e32 v163, 9, v74
	v_ashrrev_i32_e32 v164, 9, v73
	v_ashrrev_i32_e32 v165, 9, v84
	v_cmp_gt_i32_e64 s[0:1], s0, v200
	v_lshlrev_b32_e32 v72, 3, v155
	v_readfirstlane_b32 s35, v200
	s_cselect_b64 s[4:5], -1, 0
	s_cmpk_gt_i32 s34, 0x17ff
	v_mov_b32_e32 v166, 0
	s_cbranch_scc1 .LBB0_612
	s_mul_hi_i32 s26, s34, 0x2aaaaaab
	s_lshr_b32 s27, s26, 31
	s_ashr_i32 s26, s26, 6
	s_add_i32 s26, s26, s27
	s_mul_i32 s27, s26, 0x180
	s_sub_i32 s27, s34, s27
	s_ashr_i32 s37, s27, 5
	s_lshl_b32 s27, s27, 1
	s_and_b32 s36, s27, 62
	v_med3_u32 v0, s36, 4, 60
	v_mov_b64_e32 v[66:67], s[22:23]
	v_readfirstlane_b32 s27, v0
	s_add_i32 s40, s27, -4
	s_mov_b32 s99, s40
	v_add_u32_e32 v0, s40, v157
	v_add_u32_e32 v8, s40, v158
	v_add_u32_e32 v16, s40, v159
	v_add_u32_e32 v24, s40, v160
	v_add_u32_e32 v32, s40, v161
	v_add_u32_e32 v40, s40, v162
	v_add_u32_e32 v48, s40, v163
	v_add_u32_e32 v56, s40, v164
	v_add_u32_e32 v68, s40, v165
	s_ashr_i32 s27, s26, 31
	v_min_i32_e32 v0, 63, v0
	v_min_i32_e32 v8, 63, v8
	v_min_i32_e32 v16, 63, v16
	v_min_i32_e32 v24, 63, v24
	v_min_i32_e32 v32, 63, v32
	v_min_i32_e32 v40, 63, v40
	v_min_i32_e32 v48, 63, v48
	v_min_i32_e32 v56, 63, v56
	v_min_i32_e32 v68, 63, v68
	s_lshl_b64 s[28:29], s[26:27], 12
	v_lshlrev_b32_e32 v0, 6, v0
	v_lshlrev_b32_e32 v8, 6, v8
	v_lshlrev_b32_e32 v16, 6, v16
	v_lshlrev_b32_e32 v24, 6, v24
	v_lshlrev_b32_e32 v32, 6, v32
	v_lshlrev_b32_e32 v40, 6, v40
	v_lshlrev_b32_e32 v48, 6, v48
	v_lshlrev_b32_e32 v56, 6, v56
	v_lshlrev_b32_e32 v68, 6, v68
	v_mov_b32_e32 v65, s29
	v_or_b32_e32 v64, s28, v156
	v_ashrrev_i32_e32 v1, 31, v0
	v_ashrrev_i32_e32 v9, 31, v8
	v_ashrrev_i32_e32 v17, 31, v16
	v_ashrrev_i32_e32 v25, 31, v24
	v_ashrrev_i32_e32 v33, 31, v32
	v_ashrrev_i32_e32 v41, 31, v40
	v_ashrrev_i32_e32 v49, 31, v48
	v_ashrrev_i32_e32 v57, 31, v56
	v_ashrrev_i32_e32 v69, 31, v68
	s_lshl_b32 s26, s37, 6
	v_lshl_add_u64 v[0:1], v[64:65], 0, v[0:1]
	v_lshl_add_u64 v[8:9], v[64:65], 0, v[8:9]
	v_lshl_add_u64 v[16:17], v[64:65], 0, v[16:17]
	v_lshl_add_u64 v[24:25], v[64:65], 0, v[24:25]
	v_lshl_add_u64 v[32:33], v[64:65], 0, v[32:33]
	v_lshl_add_u64 v[40:41], v[64:65], 0, v[40:41]
	v_lshl_add_u64 v[48:49], v[64:65], 0, v[48:49]
	v_lshl_add_u64 v[56:57], v[64:65], 0, v[56:57]
	v_lshl_add_u64 v[64:65], v[64:65], 0, v[68:69]
	s_ashr_i32 s27, s26, 31
	v_mad_u64_u32 v[2:3], s[30:31], v0, s81, v[66:67]
	v_mad_u64_u32 v[10:11], s[38:39], v8, s81, v[66:67]
	v_mad_u64_u32 v[18:19], s[38:39], v16, s81, v[66:67]
	v_mad_u64_u32 v[26:27], s[38:39], v24, s81, v[66:67]
	v_mad_u64_u32 v[34:35], s[38:39], v32, s81, v[66:67]
	v_mad_u64_u32 v[42:43], s[38:39], v40, s81, v[66:67]
	v_mad_u64_u32 v[50:51], s[38:39], v48, s81, v[66:67]
	v_mad_u64_u32 v[58:59], s[38:39], v56, s81, v[66:67]
	v_mad_u64_u32 v[66:67], s[38:39], v64, s81, v[66:67]
	v_mad_i32_i24 v3, v1, s81, v3
	s_lshl_b64 s[30:31], s[26:27], 1
	v_mad_i32_i24 v11, v9, s81, v11
	v_mad_i32_i24 v19, v17, s81, v19
	v_mad_i32_i24 v27, v25, s81, v27
	v_mad_i32_i24 v35, v33, s81, v35
	v_mad_i32_i24 v43, v41, s81, v43
	v_mad_i32_i24 v51, v49, s81, v51
	v_mad_i32_i24 v59, v57, s81, v59
	v_mad_i32_i24 v67, v65, s81, v67
	v_lshl_add_u64 v[0:1], v[2:3], 0, s[30:31]
	v_and_b32_e32 v244, 0x70, v151
	v_lshl_add_u64 v[8:9], v[10:11], 0, s[30:31]
	v_lshl_add_u64 v[16:17], v[18:19], 0, s[30:31]
	v_lshl_add_u64 v[24:25], v[26:27], 0, s[30:31]
	v_lshl_add_u64 v[32:33], v[34:35], 0, s[30:31]
	v_lshl_add_u64 v[40:41], v[42:43], 0, s[30:31]
	v_lshl_add_u64 v[48:49], v[50:51], 0, s[30:31]
	v_lshl_add_u64 v[56:57], v[58:59], 0, s[30:31]
	v_lshl_add_u64 v[64:65], v[66:67], 0, s[30:31]
	v_lshl_add_u64 v[0:1], v[0:1], 0, v[244:245]
	v_lshl_add_u64 v[8:9], v[8:9], 0, v[244:245]
	v_lshl_add_u64 v[16:17], v[16:17], 0, v[244:245]
	v_lshl_add_u64 v[24:25], v[24:25], 0, v[244:245]
	v_lshl_add_u64 v[32:33], v[32:33], 0, v[244:245]
	v_lshl_add_u64 v[40:41], v[40:41], 0, v[244:245]
	v_lshl_add_u64 v[48:49], v[48:49], 0, v[244:245]
	v_lshl_add_u64 v[60:61], v[56:57], 0, v[244:245]
	v_lshl_add_u64 v[68:69], v[64:65], 0, v[244:245]
	global_load_dwordx4 v[4:7], v[0:1], off offset:1536
	s_nop 0
	global_load_dwordx4 v[0:3], v[0:1], off offset:3072
	s_nop 0
	global_load_dwordx4 v[12:15], v[8:9], off offset:1536
	s_nop 0
	global_load_dwordx4 v[8:11], v[8:9], off offset:3072
	s_nop 0
	global_load_dwordx4 v[20:23], v[16:17], off offset:1536
	s_nop 0
	global_load_dwordx4 v[16:19], v[16:17], off offset:3072
	s_nop 0
	global_load_dwordx4 v[28:31], v[24:25], off offset:1536
	s_nop 0
	global_load_dwordx4 v[24:27], v[24:25], off offset:3072
	s_nop 0
	global_load_dwordx4 v[36:39], v[32:33], off offset:1536
	s_nop 0
	global_load_dwordx4 v[32:35], v[32:33], off offset:3072
	s_nop 0
	global_load_dwordx4 v[44:47], v[40:41], off offset:1536
	s_nop 0
	global_load_dwordx4 v[40:43], v[40:41], off offset:3072
	s_nop 0
	global_load_dwordx4 v[52:55], v[48:49], off offset:1536
	s_nop 0
	global_load_dwordx4 v[48:51], v[48:49], off offset:3072
	s_nop 0
	global_load_dwordx4 v[56:59], v[60:61], off offset:1536
	s_nop 0
	global_load_dwordx4 v[60:63], v[60:61], off offset:3072
	s_nop 0
	global_load_dwordx4 v[64:67], v[68:69], off offset:1536
	s_nop 0
	global_load_dwordx4 v[68:71], v[68:69], off offset:3072
	v_mov_b32_e32 v166, 0
	s_and_saveexec_b64 s[30:31], s[0:1]
	s_cbranch_execz .LBB0_611
	s_mulk_i32 s37, 0x1d1
	v_add_u32_e32 v80, s37, v200
	v_ashrrev_i32_e32 v81, 31, v80
	v_lshl_add_u64 v[80:81], v[80:81], 2, s[24:25]
	global_load_dword v166, v[80:81], off

.LBB0_612:
	v_lshrrev_b32_e32 v85, 3, v200
	s_andn2_b64 vcc, exec, s[4:5]
	s_cbranch_vccnz .LBB0_752
	s_movk_i32 s4, 0x70
	v_bitop3_b32 v86, v151, s4, v200 bitop3:0x48
	v_add_u32_e32 v167, 0, v86
	v_xor_b32_e32 v86, v85, v190
	v_lshlrev_b32_e32 v86, 4, v86
	v_and_b32_e32 v86, 0x70, v86
	s_add_i32 s4, 0, 0x12000
	v_lshlrev_b32_e32 v87, 3, v200
	v_add_u32_e32 v168, s4, v86
	v_and_b32_e32 v86, 56, v87
	v_and_b32_e32 v87, 8, v87
	v_add_u32_e32 v173, s4, v87
	s_mov_b32 s4, 0x1ffffc0
	v_lshrrev_b32_e32 v73, 3, v73
	v_lshlrev_b32_e32 v88, 2, v201
	v_and_or_b32 v73, v73, s4, v156
	v_lshlrev_b32_e32 v148, 2, v155
	v_xor_b32_e32 v170, 64, v88
	v_xor_b32_e32 v171, 0x80, v88
	v_lshrrev_b32_e32 v88, 2, v154
	v_lshlrev_b32_e32 v181, 7, v73
	v_lshrrev_b32_e32 v73, 3, v84
	v_or_b32_e32 v172, v148, v88
	v_bfe_u32 v87, v190, 1, 1
	v_and_or_b32 v73, v73, s4, v156
	v_lshlrev_b32_e32 v182, 7, v73
	v_bitop3_b32 v73, v172, v87, 7 bitop3:0x6c
	v_lshlrev_b32_e32 v184, 4, v73
	v_or_b32_e32 v73, 2, v87
	v_bitop3_b32 v73, v172, v73, 7 bitop3:0x6c
	v_lshlrev_b32_e32 v185, 4, v73
	v_or_b32_e32 v73, 4, v87
	v_bitop3_b32 v73, v172, v73, 7 bitop3:0x6c
	v_lshlrev_b32_e32 v186, 4, v73
	v_or_b32_e32 v73, 6, v87
	s_bfe_u32 s56, s35, 0x20006
	s_add_i32 s5, 0, 0x24000
	v_lshrrev_b32_e32 v79, 3, v79
	v_lshrrev_b32_e32 v78, 3, v78
	v_lshrrev_b32_e32 v77, 3, v77
	v_lshrrev_b32_e32 v76, 3, v76
	v_lshrrev_b32_e32 v75, 3, v75
	v_lshrrev_b32_e32 v74, 3, v74
	v_bitop3_b32 v73, v172, v73, 7 bitop3:0x6c
	s_ashr_i32 s55, s35, 8
	v_lshl_or_b32 v150, s56, 4, v154
	v_and_or_b32 v85, v85, s4, v156
	v_and_or_b32 v79, v79, s4, v156
	v_and_or_b32 v78, v78, s4, v156
	v_and_or_b32 v77, v77, s4, v156
	v_and_or_b32 v76, v76, s4, v156
	v_and_or_b32 v75, v75, s4, v156
	v_and_or_b32 v74, v74, s4, v156
	v_lshlrev_b32_e32 v187, 4, v73
	s_cmp_eq_u32 s56, 2
	v_med3_u32 v73, v150, 8, 56
	v_lshl_add_u32 v169, v200, 2, s5
	v_mov_b32_e32 v149, v245
	v_lshlrev_b32_e32 v174, 7, v85
	v_lshlrev_b32_e32 v175, 7, v79
	v_lshlrev_b32_e32 v176, 7, v78
	v_lshlrev_b32_e32 v177, 7, v77
	v_lshlrev_b32_e32 v178, 7, v76
	v_lshlrev_b32_e32 v179, 7, v75
	v_lshlrev_b32_e32 v180, 7, v74
	v_or_b32_e32 v183, 4, v155
	s_cselect_b32 s57, 24, 32
	v_add_u32_e32 v188, -8, v73
	v_add_u32_e32 v189, 8, v73
	s_lshl_b32 s58, s34, 1
	s_lshl_b32 s59, s70, 1
	s_cmp_eq_u32 s70, 0x100
	s_cselect_b32 s59, 2, s59
	v_lshlrev_b32_e32 v244, 1, v86
	v_lshlrev_b32_e32 v152, 1, v72
	s_branch .LBB0_615

.LBB0_615:
	v_add_u32_e32 v72, v167, v174
	s_waitcnt vmcnt(0)
	s_barrier
	s_lshr_b32 s4, s99, 8
	s_cmp_eq_u32 s4, 2
	s_cbranch_scc1 .Lna_top_skip
	s_cmp_lg_u32 s4, 1
	s_cbranch_scc1 .Lna_top_write
	v_add_u32_e32 v212, v167, v176
	ds_read_b128 v[4:7], v212
	v_add_u32_e32 v213, v168, v176
	ds_read_b128 v[0:3], v213
	v_add_u32_e32 v212, v167, v177
	ds_read_b128 v[12:15], v212
	v_add_u32_e32 v213, v168, v177
	ds_read_b128 v[8:11], v213
	v_add_u32_e32 v212, v167, v178
	ds_read_b128 v[20:23], v212
	v_add_u32_e32 v213, v168, v178
	ds_read_b128 v[16:19], v213
	v_add_u32_e32 v212, v167, v179
	ds_read_b128 v[28:31], v212
	v_add_u32_e32 v213, v168, v179
	ds_read_b128 v[24:27], v213
	v_add_u32_e32 v212, v167, v180
	ds_read_b128 v[36:39], v212
	v_add_u32_e32 v213, v168, v180
	ds_read_b128 v[32:35], v213
	v_add_u32_e32 v212, v167, v181
	ds_read_b128 v[44:47], v212
	v_add_u32_e32 v213, v168, v181
	ds_read_b128 v[40:43], v213
	v_add_u32_e32 v212, v167, v182
	ds_read_b128 v[52:55], v212
	v_add_u32_e32 v213, v168, v182
	ds_read_b128 v[48:51], v213
	s_waitcnt lgkmcnt(0)
.Lna_top_write:
	ds_write_b128 v72, v[4:7]
	v_add_u32_e32 v4, v168, v174
	ds_write_b128 v4, v[0:3]
	v_add_u32_e32 v0, v167, v175
	ds_write_b128 v0, v[12:15]
	v_add_u32_e32 v0, v168, v175
	ds_write_b128 v0, v[8:11]
	v_add_u32_e32 v0, v167, v176
	ds_write_b128 v0, v[20:23]
	v_add_u32_e32 v0, v168, v176
	ds_write_b128 v0, v[16:19]
	v_add_u32_e32 v0, v167, v177
	ds_write_b128 v0, v[28:31]
	v_add_u32_e32 v0, v168, v177
	ds_write_b128 v0, v[24:27]
	v_add_u32_e32 v0, v167, v178
	ds_write_b128 v0, v[36:39]
	v_add_u32_e32 v0, v168, v178
	ds_write_b128 v0, v[32:35]
	v_add_u32_e32 v0, v167, v179
	ds_write_b128 v0, v[44:47]
	v_add_u32_e32 v0, v168, v179
	ds_write_b128 v0, v[40:43]
	v_add_u32_e32 v0, v167, v180
	ds_write_b128 v0, v[52:55]
	v_add_u32_e32 v0, v168, v180
	ds_write_b128 v0, v[48:51]
	v_add_u32_e32 v0, v167, v181
	ds_write_b128 v0, v[56:59]
	v_add_u32_e32 v0, v168, v181
	ds_write_b128 v0, v[60:63]
	v_add_u32_e32 v0, v167, v182
	ds_write_b128 v0, v[64:67]
	v_add_u32_e32 v0, v168, v182
	ds_write_b128 v0, v[68:71]
.Lna_top_skip:
	s_and_saveexec_b64 s[4:5], s[0:1]
	v_mul_f32_e32 v0, 0x3fb8aa3b, v166
	ds_write_b32 v169, v0
	s_or_b64 exec, exec, s[4:5]
	s_lshr_b32 s60, s59, 1
	s_add_i32 s60, s60, s34
	s_cmp_ge_i32 s60, s98
	s_cselect_b64 s[26:27], -1, 0
	s_cmp_lt_i32 s60, s98
	s_cselect_b32 s5, s60, s34
	s_mul_hi_i32 s4, s5, 0x2aaaaaab
	s_lshr_b32 s28, s4, 31
	s_ashr_i32 s4, s4, 6
	s_add_i32 s4, s4, s28
	s_mul_i32 s28, s4, 0x180
	s_sub_i32 s5, s5, s28
	s_ashr_i32 s36, s5, 5
	s_lshl_b32 s5, s5, 1
	s_and_b32 s35, s5, 62
	v_med3_u32 v0, s35, 4, 60
	v_mov_b64_e32 v[66:67], s[22:23]
	v_readfirstlane_b32 s5, v0
	s_add_i32 s37, s5, -4
	s_and_b32 s28, s99, 0xff
	s_mov_b32 s99, s37
	s_cmp_lg_u32 s70, 0x100
	s_cbranch_scc1 .Lna_mode_done
	s_cmp_eq_u32 s35, 0
	s_cbranch_scc1 .Lna_mode_done
	s_or_b32 s99, s37, 0x100
	s_cmp_lg_u32 s37, s28
	s_cbranch_scc1 .Lna_mode_done
	s_or_b32 s99, s37, 0x200
.Lna_mode_done:
	s_ashr_i32 s5, s4, 31
	s_lshl_b64 s[30:31], s[4:5], 12
	s_lshl_b32 s4, s36, 6
	s_ashr_i32 s5, s4, 31
	s_lshl_b64 s[28:29], s[4:5], 1
	v_mov_b32_e32 v65, s31
	v_or_b32_e32 v64, s30, v156
	s_lshr_b32 vcc_lo, s99, 8
	s_cmp_lg_u32 vcc_lo, 0
	s_cbranch_scc1 .Lna_addr_partial
	v_add_u32_e32 v0, s37, v157
	v_add_u32_e32 v8, s37, v158
	v_add_u32_e32 v16, s37, v159
	v_add_u32_e32 v24, s37, v160
	v_add_u32_e32 v32, s37, v161
	v_add_u32_e32 v40, s37, v162
	v_add_u32_e32 v48, s37, v163
	v_min_i32_e32 v0, 63, v0
	v_min_i32_e32 v8, 63, v8
	v_min_i32_e32 v16, 63, v16
	v_min_i32_e32 v24, 63, v24
	v_min_i32_e32 v32, 63, v32
	v_min_i32_e32 v40, 63, v40
	v_min_i32_e32 v48, 63, v48
	v_lshlrev_b32_e32 v0, 6, v0
	v_lshlrev_b32_e32 v8, 6, v8
	v_lshlrev_b32_e32 v16, 6, v16
	v_lshlrev_b32_e32 v24, 6, v24
	v_lshlrev_b32_e32 v32, 6, v32
	v_lshlrev_b32_e32 v40, 6, v40
	v_lshlrev_b32_e32 v48, 6, v48
	v_ashrrev_i32_e32 v1, 31, v0
	v_ashrrev_i32_e32 v9, 31, v8
	v_ashrrev_i32_e32 v17, 31, v16
	v_ashrrev_i32_e32 v25, 31, v24
	v_ashrrev_i32_e32 v33, 31, v32
	v_ashrrev_i32_e32 v41, 31, v40
	v_ashrrev_i32_e32 v49, 31, v48
	v_lshl_add_u64 v[0:1], v[64:65], 0, v[0:1]
	v_lshl_add_u64 v[8:9], v[64:65], 0, v[8:9]
	v_lshl_add_u64 v[16:17], v[64:65], 0, v[16:17]
	v_lshl_add_u64 v[24:25], v[64:65], 0, v[24:25]
	v_lshl_add_u64 v[32:33], v[64:65], 0, v[32:33]
	v_lshl_add_u64 v[40:41], v[64:65], 0, v[40:41]
	v_lshl_add_u64 v[48:49], v[64:65], 0, v[48:49]
	v_mad_u64_u32 v[2:3], s[38:39], v0, s81, v[66:67]
	v_mad_u64_u32 v[10:11], s[38:39], v8, s81, v[66:67]
	v_mad_u64_u32 v[18:19], s[38:39], v16, s81, v[66:67]
	v_mad_u64_u32 v[26:27], s[38:39], v24, s81, v[66:67]
	v_mad_u64_u32 v[34:35], s[38:39], v32, s81, v[66:67]
	v_mad_u64_u32 v[42:43], s[38:39], v40, s81, v[66:67]
	v_mad_u64_u32 v[50:51], s[38:39], v48, s81, v[66:67]
	v_mad_i32_i24 v3, v1, s81, v3
	v_mad_i32_i24 v11, v9, s81, v11
	v_mad_i32_i24 v19, v17, s81, v19
	v_mad_i32_i24 v27, v25, s81, v27
	v_mad_i32_i24 v35, v33, s81, v35
	v_mad_i32_i24 v43, v41, s81, v43
	v_mad_i32_i24 v51, v49, s81, v51
	v_lshl_add_u64 v[0:1], v[2:3], 0, s[28:29]
	v_lshl_add_u64 v[8:9], v[10:11], 0, s[28:29]
	v_lshl_add_u64 v[16:17], v[18:19], 0, s[28:29]
	v_lshl_add_u64 v[24:25], v[26:27], 0, s[28:29]
	v_lshl_add_u64 v[32:33], v[34:35], 0, s[28:29]
	v_lshl_add_u64 v[40:41], v[42:43], 0, s[28:29]
	v_lshl_add_u64 v[48:49], v[50:51], 0, s[28:29]
	v_lshl_add_u64 v[0:1], v[0:1], 0, v[244:245]
	v_lshl_add_u64 v[8:9], v[8:9], 0, v[244:245]
	v_lshl_add_u64 v[16:17], v[16:17], 0, v[244:245]
	v_lshl_add_u64 v[24:25], v[24:25], 0, v[244:245]
	v_lshl_add_u64 v[32:33], v[32:33], 0, v[244:245]
	v_lshl_add_u64 v[40:41], v[40:41], 0, v[244:245]
	v_lshl_add_u64 v[48:49], v[48:49], 0, v[244:245]
.Lna_addr_partial:
	v_add_u32_e32 v56, s37, v164
	v_add_u32_e32 v68, s37, v165
	v_min_i32_e32 v56, 63, v56
	v_min_i32_e32 v68, 63, v68
	v_lshlrev_b32_e32 v56, 6, v56
	v_lshlrev_b32_e32 v68, 6, v68
	v_ashrrev_i32_e32 v57, 31, v56
	v_ashrrev_i32_e32 v69, 31, v68
	v_lshl_add_u64 v[56:57], v[64:65], 0, v[56:57]
	v_lshl_add_u64 v[64:65], v[64:65], 0, v[68:69]
	v_mad_u64_u32 v[58:59], s[38:39], v56, s81, v[66:67]
	v_mad_u64_u32 v[66:67], s[38:39], v64, s81, v[66:67]
	v_mad_i32_i24 v59, v57, s81, v59
	v_mad_i32_i24 v67, v65, s81, v67
	v_lshl_add_u64 v[56:57], v[58:59], 0, s[28:29]
	v_lshl_add_u64 v[64:65], v[66:67], 0, s[28:29]
	v_lshl_add_u64 v[60:61], v[56:57], 0, v[244:245]
	v_lshl_add_u64 v[68:69], v[64:65], 0, v[244:245]
	s_waitcnt lgkmcnt(0)
	s_barrier
	s_lshr_b32 s28, s99, 8
	s_cmp_lg_u32 s28, 0
	s_cbranch_scc1 .Lna_ld_partial
	global_load_dwordx4 v[4:7], v[0:1], off offset:1536
	s_nop 0
	global_load_dwordx4 v[0:3], v[0:1], off offset:3072
	s_nop 0
	global_load_dwordx4 v[12:15], v[8:9], off offset:1536
	s_nop 0
	global_load_dwordx4 v[8:11], v[8:9], off offset:3072
	s_nop 0
	global_load_dwordx4 v[20:23], v[16:17], off offset:1536
	s_nop 0
	global_load_dwordx4 v[16:19], v[16:17], off offset:3072
	s_nop 0
	global_load_dwordx4 v[28:31], v[24:25], off offset:1536
	s_nop 0
	global_load_dwordx4 v[24:27], v[24:25], off offset:3072
	s_nop 0
	global_load_dwordx4 v[36:39], v[32:33], off offset:1536
	s_nop 0
	global_load_dwordx4 v[32:35], v[32:33], off offset:3072
	s_nop 0
	global_load_dwordx4 v[44:47], v[40:41], off offset:1536
	s_nop 0
	global_load_dwordx4 v[40:43], v[40:41], off offset:3072
	s_nop 0
	global_load_dwordx4 v[52:55], v[48:49], off offset:1536
	s_nop 0
	global_load_dwordx4 v[48:51], v[48:49], off offset:3072
	s_nop 0
.Lna_ld_partial:
	s_cmp_eq_u32 s28, 2
	s_cbranch_scc1 .Lna_ld_none
	global_load_dwordx4 v[56:59], v[60:61], off offset:1536
	s_nop 0
	global_load_dwordx4 v[60:63], v[60:61], off offset:3072
	s_nop 0
	global_load_dwordx4 v[64:67], v[68:69], off offset:1536
	s_nop 0
	global_load_dwordx4 v[68:71], v[68:69], off offset:3072
.Lna_ld_none:
	s_and_saveexec_b64 s[28:29], s[0:1]
	s_cbranch_execz .LBB0_619
	s_mulk_i32 s36, 0x1d1
	v_add_u32_e32 v72, s36, v200
	v_ashrrev_i32_e32 v73, 31, v72
	v_lshl_add_u64 v[72:73], v[72:73], 2, s[24:25]
	global_load_dword v166, v[72:73], off
